# baseline (speedup 1.0000x reference)
.LBB1_13:
	v_mfma_f32_32x32x16_bf16 v[2:17], v[78:81], v[206:209], v[236:251]
	ds_read_b128 v[174:177], v210
	v_add_u32_e32 v195, v230, v228
	v_mfma_f32_32x32x16_bf16 v[2:17], v[74:77], v[190:193], v[2:17]
	ds_read_b128 v[170:173], v210 offset:1024
	v_exp_f32_e32 v199, v28
	v_exp_f32_e32 v198, v32
	v_exp_f32_e32 v197, v20
	v_exp_f32_e32 v196, v24
	v_mfma_f32_32x32x16_bf16 v[2:17], v[70:73], v[158:161], v[2:17]
	ds_read_b128 v[166:169], v210 offset:2048
	v_exp_f32_e32 v18, v18
	v_exp_f32_e32 v22, v22
	v_exp_f32_e32 v24, v26
	v_exp_f32_e32 v26, v30
	v_fma_f32 v20, v197, s12, s12
	v_fma_f32 v28, v196, s12, s12
	v_fma_f32 v30, v199, s12, s12
	v_fma_f32 v32, v198, s12, s12
	v_mfma_f32_32x32x16_bf16 v[2:17], v[66:69], v[142:145], v[2:17]
	ds_read_b128 v[162:165], v210 offset:3072
	v_exp_f32_e32 v19, v19
	v_exp_f32_e32 v23, v23
	v_exp_f32_e32 v27, v27
	v_exp_f32_e32 v31, v31
	v_fmac_f32_e32 v20, v18, v20
	v_fmac_f32_e32 v28, v22, v28
	v_fmac_f32_e32 v30, v24, v30
	v_fmac_f32_e32 v32, v26, v32
	v_mfma_f32_32x32x16_bf16 v[2:17], v[62:65], v[154:157], v[2:17]
	ds_read_b128 v[158:161], v210 offset:4096
	v_add_f32_e32 v22, 1.0, v19
	v_rcp_f32_e32 v19, v20
	v_rcp_f32_e32 v18, v28
	v_add_f32_e32 v20, 1.0, v23
	v_rcp_f32_e32 v191, v30
	v_rcp_f32_e32 v190, v32
	v_mfma_f32_32x32x16_bf16 v[2:17], v[58:61], v[182:185], v[2:17]
	ds_read_b128 v[154:157], v210 offset:5120
	v_exp_f32_e32 v206, v21
	v_exp_f32_e32 v207, v25
	v_add_f32_e32 v23, 1.0, v27
	v_rcp_f32_e32 v192, v20
	v_add_f32_e32 v20, 1.0, v31
	v_rcp_f32_e32 v193, v22
	v_mfma_f32_32x32x16_bf16 v[2:17], v[54:57], v[186:189], v[2:17]
	ds_read_b128 v[142:145], v210 offset:6144
	v_exp_f32_e32 v208, v29
	v_exp_f32_e32 v209, v33
	v_rcp_f32_e32 v183, v23
	v_rcp_f32_e32 v182, v20
	v_mfma_f32_32x32x16_bf16 v[2:17], v[50:53], v[134:137], v[2:17]
	ds_read_b128 v[130:133], v210 offset:7168
	v_fma_f32 v186, -v196, v18, v18
	v_fma_f32 v187, -v197, v19, v19
	ds_read_b128 v[18:21], v231 offset:36928
	ds_read_b128 v[22:25], v231 offset:36944
	ds_read_b128 v[26:29], v231 offset:36960
	ds_read_b128 v[30:33], v231 offset:36976
	v_pk_fma_f32 v[134:135], v[198:199], v[190:191], v[190:191] neg_lo:[1,0,0] neg_hi:[1,0,0]
	v_pk_fma_f32 v[200:201], v[192:193], v[220:221], v[186:187]
	v_pk_fma_f32 v[198:199], v[182:183], v[222:223], v[134:135]
	v_mfma_f32_32x32x16_bf16 v[2:17], v[46:49], v[138:141], v[2:17]
	ds_read_b128 v[134:137], v195 offset:16384
	v_add_f32_e32 v182, 1.0, v206
	v_exp_f32_e32 v183, v201
	v_exp_f32_e32 v186, v200
	v_exp_f32_e32 v187, v199
	v_exp_f32_e32 v188, v198
	v_add_f32_e32 v189, 1.0, v207
	v_add_f32_e32 v190, 1.0, v208
	v_add_f32_e32 v191, 1.0, v209
	v_mfma_f32_32x32x16_bf16 v[2:17], v[42:45], v[146:149], v[2:17]
	ds_read_b128 v[138:141], v195 offset:16416
	v_fmac_f32_e32 v182, v182, v183
	v_fmac_f32_e32 v189, v189, v186
	v_fmac_f32_e32 v190, v190, v187
	v_fmac_f32_e32 v191, v191, v188
	v_mfma_f32_32x32x16_bf16 v[2:17], v[38:41], v[150:153], v[2:17]
	ds_read_b128 v[146:149], v195 offset:16448
	v_rcp_f32_e32 v182, v182
	v_rcp_f32_e32 v189, v189
	v_rcp_f32_e32 v190, v190
	v_rcp_f32_e32 v191, v191
	v_mfma_f32_32x32x16_bf16 v[2:17], v[34:37], v[178:181], v[2:17]
	ds_read_b128 v[150:153], v195 offset:16480
	v_fma_f32 v182, -v183, v182, v182
	v_fma_f32 v183, -v186, v189, v189
	v_fma_f32 v186, -v187, v190, v190
	v_fma_f32 v187, -v188, v191, v191
	s_waitcnt lgkmcnt(4)
	v_mfma_f32_32x32x16_bf16 v[18:33], v[126:129], v[174:177], v[18:33]
	v_cvt_pk_bf16_f32 v252, v182, v183
	v_cvt_pk_bf16_f32 v253, v186, v187
	v_mfma_f32_32x32x16_bf16 v[18:33], v[122:125], v[170:173], v[18:33]
	s_nop 1
	v_exp_f32_e32 v179, v4
	v_exp_f32_e32 v178, v8
	v_exp_f32_e32 v181, v12
	v_exp_f32_e32 v180, v16
	v_mfma_f32_32x32x16_bf16 v[18:33], v[118:121], v[166:169], v[18:33]
	v_exp_f32_e32 v2, v2
	v_exp_f32_e32 v6, v6
	v_exp_f32_e32 v10, v10
	v_exp_f32_e32 v12, v14
	v_fma_f32 v4, v179, s12, s12
	v_fma_f32 v8, v178, s12, s12
	v_fma_f32 v14, v181, s12, s12
	v_fma_f32 v16, v180, s12, s12
	v_mfma_f32_32x32x16_bf16 v[18:33], v[114:117], v[162:165], v[18:33]
	v_exp_f32_e32 v3, v3
	v_fmac_f32_e32 v4, v2, v4
	v_exp_f32_e32 v2, v7
	v_fmac_f32_e32 v8, v6, v8
	v_exp_f32_e32 v6, v11
	v_exp_f32_e32 v7, v15
	v_fmac_f32_e32 v14, v10, v14
	v_fmac_f32_e32 v16, v12, v16
	v_mfma_f32_32x32x16_bf16 v[18:33], v[110:113], v[158:161], v[18:33]
	v_add_f32_e32 v10, 1.0, v3
	v_rcp_f32_e32 v3, v4
	v_add_f32_e32 v4, 1.0, v2
	v_rcp_f32_e32 v2, v8
	v_rcp_f32_e32 v183, v14
	v_rcp_f32_e32 v182, v16
	v_mfma_f32_32x32x16_bf16 v[18:33], v[106:109], v[154:157], v[18:33]
	v_add_f32_e32 v6, 1.0, v6
	v_add_f32_e32 v7, 1.0, v7
	v_rcp_f32_e32 v187, v10
	v_rcp_f32_e32 v186, v4
	v_exp_f32_e32 v190, v5
	v_exp_f32_e32 v191, v9
	v_mfma_f32_32x32x16_bf16 v[18:33], v[102:105], v[142:145], v[18:33]
	v_rcp_f32_e32 v189, v6
	v_rcp_f32_e32 v188, v7
	v_exp_f32_e32 v192, v13
	v_exp_f32_e32 v193, v17
	v_mfma_f32_32x32x16_bf16 v[18:33], v[98:101], v[130:133], v[18:33]
	v_fma_f32 v178, -v178, v2, v2
	v_fma_f32 v179, -v179, v3, v3
	v_pk_fma_f32 v[206:207], v[186:187], v[216:217], v[178:179]
	v_pk_fma_f32 v[178:179], v[180:181], v[182:183], v[182:183] neg_lo:[1,0,0] neg_hi:[1,0,0]
	s_waitcnt lgkmcnt(0)
	v_mfma_f32_32x32x16_bf16 v[18:33], v[94:97], v[134:137], v[18:33]
	v_pk_fma_f32 v[208:209], v[188:189], v[218:219], v[178:179]
	v_add_f32_e32 v178, 1.0, v190
	v_exp_f32_e32 v179, v207
	v_add_f32_e32 v180, 1.0, v191
	v_exp_f32_e32 v181, v206
	v_exp_f32_e32 v182, v209
	v_exp_f32_e32 v183, v208
	v_add_f32_e32 v184, 1.0, v192
	v_add_f32_e32 v185, 1.0, v193
	v_mfma_f32_32x32x16_bf16 v[18:33], v[90:93], v[138:141], v[18:33]
	v_fmac_f32_e32 v178, v178, v179
	v_fmac_f32_e32 v180, v180, v181
	v_fmac_f32_e32 v184, v184, v182
	v_fmac_f32_e32 v185, v185, v183
	v_mfma_f32_32x32x16_bf16 v[18:33], v[86:89], v[146:149], v[18:33]
	v_rcp_f32_e32 v178, v178
	v_rcp_f32_e32 v180, v180
	v_rcp_f32_e32 v184, v184
	v_rcp_f32_e32 v185, v185
	v_mfma_f32_32x32x16_bf16 v[18:33], v[82:85], v[150:153], v[18:33]
	v_fma_f32 v178, -v179, v178, v178
	v_fma_f32 v179, -v181, v180, v180
	v_fma_f32 v180, -v182, v184, v184
	v_fma_f32 v181, -v183, v185, v185
	v_cvt_pk_bf16_f32 v254, v178, v179
	v_cvt_pk_bf16_f32 v255, v180, v181
	ds_write_b128 v211, v[252:255] offset:8192
	s_waitcnt lgkmcnt(0)
	s_barrier
	s_add_i32 s1, s1, 2
	s_cmp_gt_u32 s1, 16
	v_add_u32_e32 v232, 0x200, v232
	s_cbranch_scc1 .LBB1_30
.LBB1_14:
	v_mfma_f32_32x32x16_bf16 v[2:17], v[78:81], v[174:177], v[236:251]
	v_add_u32_e32 v192, v230, v229
	ds_read2_b32 v[228:229], v232 offset1:32
	ds_read_b128 v[194:197], v210 offset:8192
	v_mfma_f32_32x32x16_bf16 v[2:17], v[74:77], v[170:173], v[2:17]
	ds_read_b128 v[178:181], v210 offset:9216
	v_exp_f32_e32 v187, v20
	v_exp_f32_e32 v186, v24
	v_exp_f32_e32 v189, v28
	v_exp_f32_e32 v188, v32
	v_mfma_f32_32x32x16_bf16 v[2:17], v[70:73], v[166:169], v[2:17]
	ds_read_b128 v[170:173], v210 offset:10240
	v_exp_f32_e32 v18, v18
	v_exp_f32_e32 v22, v22
	v_exp_f32_e32 v24, v26
	v_exp_f32_e32 v26, v30
	v_fma_f32 v20, v187, s12, s12
	v_fma_f32 v28, v186, s12, s12
	v_fma_f32 v30, v189, s12, s12
	v_fma_f32 v32, v188, s12, s12
	v_mfma_f32_32x32x16_bf16 v[2:17], v[66:69], v[162:165], v[2:17]
	ds_read_b128 v[166:169], v210 offset:11264
	v_exp_f32_e32 v19, v19
	v_exp_f32_e32 v23, v23
	v_exp_f32_e32 v27, v27
	v_exp_f32_e32 v31, v31
	v_fmac_f32_e32 v20, v18, v20
	v_fmac_f32_e32 v28, v22, v28
	v_fmac_f32_e32 v30, v24, v30
	v_fmac_f32_e32 v32, v26, v32
	v_mfma_f32_32x32x16_bf16 v[2:17], v[62:65], v[158:161], v[2:17]
	ds_read_b128 v[162:165], v210 offset:12288
	v_add_f32_e32 v22, 1.0, v19
	v_rcp_f32_e32 v19, v20
	v_rcp_f32_e32 v18, v28
	v_rcp_f32_e32 v191, v30
	v_rcp_f32_e32 v190, v32
	v_add_f32_e32 v20, 1.0, v23
	v_mfma_f32_32x32x16_bf16 v[2:17], v[58:61], v[154:157], v[2:17]
	ds_read_b128 v[174:177], v210 offset:13312
	v_rcp_f32_e32 v159, v22
	v_rcp_f32_e32 v158, v20
	v_exp_f32_e32 v160, v21
	v_exp_f32_e32 v161, v25
	v_add_f32_e32 v23, 1.0, v27
	v_add_f32_e32 v20, 1.0, v31
	v_mfma_f32_32x32x16_bf16 v[2:17], v[54:57], v[142:145], v[2:17]
	ds_read_b128 v[182:185], v210 offset:14336
	v_rcp_f32_e32 v155, v23
	v_rcp_f32_e32 v154, v20
	v_exp_f32_e32 v193, v29
	v_exp_f32_e32 v217, v33
	v_mfma_f32_32x32x16_bf16 v[2:17], v[50:53], v[130:133], v[2:17]
	ds_read_b128 v[142:145], v210 offset:15360
	v_fma_f32 v156, -v186, v18, v18
	v_fma_f32 v157, -v187, v19, v19
	ds_read_b128 v[18:21], v231 offset:36928
	ds_read_b128 v[22:25], v231 offset:36944
	ds_read_b128 v[26:29], v231 offset:36960
	ds_read_b128 v[30:33], v231 offset:36976
	v_pk_fma_f32 v[130:131], v[188:189], v[190:191], v[190:191] neg_lo:[1,0,0] neg_hi:[1,0,0]
	v_pk_fma_f32 v[214:215], v[158:159], v[214:215], v[156:157]
	v_pk_fma_f32 v[212:213], v[154:155], v[212:213], v[130:131]
	v_mfma_f32_32x32x16_bf16 v[2:17], v[46:49], v[134:137], v[2:17]
	ds_read_b128 v[154:157], v192 offset:16384
	v_add_f32_e32 v130, 1.0, v160
	v_exp_f32_e32 v131, v215
	v_exp_f32_e32 v132, v214
	v_exp_f32_e32 v133, v213
	v_exp_f32_e32 v220, v212
	v_add_f32_e32 v134, 1.0, v161
	v_add_f32_e32 v135, 1.0, v193
	v_add_f32_e32 v136, 1.0, v217
	v_mfma_f32_32x32x16_bf16 v[2:17], v[42:45], v[138:141], v[2:17]
	ds_read_b128 v[158:161], v192 offset:16416
	v_fmac_f32_e32 v130, v130, v131
	v_fmac_f32_e32 v134, v134, v132
	v_fmac_f32_e32 v135, v135, v133
	v_fmac_f32_e32 v136, v136, v220
	v_mfma_f32_32x32x16_bf16 v[2:17], v[38:41], v[146:149], v[2:17]
	ds_read_b128 v[186:189], v192 offset:16448
	v_rcp_f32_e32 v130, v130
	v_rcp_f32_e32 v134, v134
	v_rcp_f32_e32 v135, v135
	v_rcp_f32_e32 v136, v136
	v_mfma_f32_32x32x16_bf16 v[2:17], v[34:37], v[150:153], v[2:17]
	ds_read_b128 v[190:193], v192 offset:16480
	v_fma_f32 v130, -v131, v130, v130
	v_fma_f32 v131, -v132, v134, v134
	v_fma_f32 v132, -v133, v135, v135
	v_fma_f32 v133, -v220, v136, v136
	s_waitcnt lgkmcnt(4)
	v_mfma_f32_32x32x16_bf16 v[18:33], v[126:129], v[194:197], v[18:33]
	v_cvt_pk_bf16_f32 v252, v130, v131
	v_cvt_pk_bf16_f32 v253, v132, v133
	v_mfma_f32_32x32x16_bf16 v[18:33], v[122:125], v[178:181], v[18:33]
	s_nop 1
	v_exp_f32_e32 v131, v4
	v_exp_f32_e32 v130, v8
	v_exp_f32_e32 v133, v12
	v_exp_f32_e32 v132, v16
	v_mfma_f32_32x32x16_bf16 v[18:33], v[118:121], v[170:173], v[18:33]
	v_exp_f32_e32 v2, v2
	v_exp_f32_e32 v6, v6
	v_exp_f32_e32 v10, v10
	v_exp_f32_e32 v12, v14
	v_fma_f32 v4, v131, s12, s12
	v_fma_f32 v8, v130, s12, s12
	v_fma_f32 v14, v133, s12, s12
	v_fma_f32 v16, v132, s12, s12
	v_mfma_f32_32x32x16_bf16 v[18:33], v[114:117], v[166:169], v[18:33]
	v_exp_f32_e32 v3, v3
	v_fmac_f32_e32 v4, v2, v4
	v_exp_f32_e32 v2, v7
	v_fmac_f32_e32 v8, v6, v8
	v_exp_f32_e32 v6, v11
	v_exp_f32_e32 v7, v15
	v_fmac_f32_e32 v14, v10, v14
	v_fmac_f32_e32 v16, v12, v16
	v_mfma_f32_32x32x16_bf16 v[18:33], v[110:113], v[162:165], v[18:33]
	v_add_f32_e32 v10, 1.0, v3
	v_rcp_f32_e32 v3, v4
	v_add_f32_e32 v4, 1.0, v2
	v_rcp_f32_e32 v2, v8
	v_rcp_f32_e32 v135, v14
	v_rcp_f32_e32 v134, v16
	v_mfma_f32_32x32x16_bf16 v[18:33], v[106:109], v[174:177], v[18:33]
	v_add_f32_e32 v6, 1.0, v6
	v_add_f32_e32 v7, 1.0, v7
	v_rcp_f32_e32 v137, v10
	v_rcp_f32_e32 v136, v4
	v_exp_f32_e32 v140, v5
	v_exp_f32_e32 v141, v9
	v_mfma_f32_32x32x16_bf16 v[18:33], v[102:105], v[182:185], v[18:33]
	v_rcp_f32_e32 v139, v6
	v_rcp_f32_e32 v138, v7
	v_exp_f32_e32 v146, v13
	v_exp_f32_e32 v147, v17
	v_mfma_f32_32x32x16_bf16 v[18:33], v[98:101], v[142:145], v[18:33]
	v_fma_f32 v130, -v130, v2, v2
	v_fma_f32 v131, -v131, v3, v3
	v_pk_fma_f32 v[224:225], v[136:137], v[204:205], v[130:131]
	v_pk_fma_f32 v[130:131], v[132:133], v[134:135], v[134:135] neg_lo:[1,0,0] neg_hi:[1,0,0]
	s_waitcnt lgkmcnt(0)
	v_mfma_f32_32x32x16_bf16 v[18:33], v[94:97], v[154:157], v[18:33]
	v_pk_fma_f32 v[226:227], v[138:139], v[202:203], v[130:131]
	v_add_f32_e32 v130, 1.0, v140
	v_exp_f32_e32 v131, v225
	v_add_f32_e32 v132, 1.0, v141
	v_exp_f32_e32 v133, v224
	v_exp_f32_e32 v134, v227
	v_exp_f32_e32 v135, v226
	v_add_f32_e32 v136, 1.0, v146
	v_add_f32_e32 v137, 1.0, v147
	v_mfma_f32_32x32x16_bf16 v[18:33], v[90:93], v[158:161], v[18:33]
	v_fmac_f32_e32 v130, v130, v131
	v_fmac_f32_e32 v132, v132, v133
	v_fmac_f32_e32 v136, v136, v134
	v_fmac_f32_e32 v137, v137, v135
	v_mfma_f32_32x32x16_bf16 v[18:33], v[86:89], v[186:189], v[18:33]
	v_rcp_f32_e32 v130, v130
	v_rcp_f32_e32 v132, v132
	v_rcp_f32_e32 v136, v136
	v_rcp_f32_e32 v137, v137
	v_mfma_f32_32x32x16_bf16 v[18:33], v[82:85], v[190:193], v[18:33]
	v_fma_f32 v130, -v131, v130, v130
	v_fma_f32 v131, -v133, v132, v132
	v_fma_f32 v132, -v134, v136, v136
	v_fma_f32 v133, -v135, v137, v137
	v_cvt_pk_bf16_f32 v254, v130, v131
	v_cvt_pk_bf16_f32 v255, v132, v133
	ds_write_b128 v211, v[252:255] offset:0
	s_waitcnt lgkmcnt(0)
	s_barrier
	v_mfma_f32_32x32x16_bf16 v[2:17], v[78:81], v[194:197], v[236:251]
	ds_read_b128 v[202:205], v210
	v_add_u32_e32 v216, v230, v228
	v_mfma_f32_32x32x16_bf16 v[2:17], v[74:77], v[178:181], v[2:17]
	ds_read_b128 v[194:197], v210 offset:1024
	v_exp_f32_e32 v147, v20
	v_exp_f32_e32 v146, v24
	v_exp_f32_e32 v149, v28
	v_exp_f32_e32 v148, v32
	v_mfma_f32_32x32x16_bf16 v[2:17], v[70:73], v[170:173], v[2:17]
	ds_read_b128 v[138:141], v210 offset:2048
	v_exp_f32_e32 v18, v18
	v_exp_f32_e32 v22, v22
	v_exp_f32_e32 v24, v26
	v_exp_f32_e32 v26, v30
	v_fma_f32 v20, v147, s12, s12
	v_fma_f32 v28, v146, s12, s12
	v_fma_f32 v30, v149, s12, s12
	v_fma_f32 v32, v148, s12, s12
	v_mfma_f32_32x32x16_bf16 v[2:17], v[66:69], v[166:169], v[2:17]
	ds_read_b128 v[134:137], v210 offset:3072
	v_exp_f32_e32 v19, v19
	v_exp_f32_e32 v23, v23
	v_exp_f32_e32 v27, v27
	v_exp_f32_e32 v31, v31
	v_fmac_f32_e32 v20, v18, v20
	v_fmac_f32_e32 v28, v22, v28
	v_fmac_f32_e32 v30, v24, v30
	v_fmac_f32_e32 v32, v26, v32
	v_mfma_f32_32x32x16_bf16 v[2:17], v[62:65], v[162:165], v[2:17]
	ds_read_b128 v[166:169], v210 offset:4096
	v_add_f32_e32 v22, 1.0, v19
	v_rcp_f32_e32 v19, v20
	v_rcp_f32_e32 v18, v28
	v_rcp_f32_e32 v151, v30
	v_rcp_f32_e32 v150, v32
	v_add_f32_e32 v20, 1.0, v23
	v_mfma_f32_32x32x16_bf16 v[2:17], v[58:61], v[174:177], v[2:17]
	ds_read_b128 v[162:165], v210 offset:5120
	v_rcp_f32_e32 v153, v22
	v_rcp_f32_e32 v152, v20
	v_add_f32_e32 v23, 1.0, v27
	v_add_f32_e32 v20, 1.0, v31
	v_exp_f32_e32 v180, v21
	v_exp_f32_e32 v181, v25
	v_mfma_f32_32x32x16_bf16 v[2:17], v[54:57], v[182:185], v[2:17]
	ds_read_b128 v[170:173], v210 offset:6144
	v_rcp_f32_e32 v175, v23
	v_rcp_f32_e32 v174, v20
	v_exp_f32_e32 v176, v29
	v_exp_f32_e32 v177, v33
	v_mfma_f32_32x32x16_bf16 v[2:17], v[50:53], v[142:145], v[2:17]
	ds_read_b128 v[130:133], v210 offset:7168
	v_fma_f32 v146, -v146, v18, v18
	v_fma_f32 v147, -v147, v19, v19
	ds_read_b128 v[18:21], v231 offset:36928
	ds_read_b128 v[22:25], v231 offset:36944
	ds_read_b128 v[26:29], v231 offset:36960
	ds_read_b128 v[30:33], v231 offset:36976
	v_pk_fma_f32 v[142:143], v[148:149], v[150:151], v[150:151] neg_lo:[1,0,0] neg_hi:[1,0,0]
	v_pk_fma_f32 v[220:221], v[152:153], v[200:201], v[146:147]
	v_pk_fma_f32 v[222:223], v[174:175], v[198:199], v[142:143]
	v_mfma_f32_32x32x16_bf16 v[2:17], v[46:49], v[154:157], v[2:17]
	ds_read_b128 v[146:149], v216 offset:16384
	v_add_f32_e32 v142, 1.0, v180
	v_exp_f32_e32 v143, v221
	v_exp_f32_e32 v144, v220
	v_exp_f32_e32 v145, v223
	v_exp_f32_e32 v180, v222
	v_add_f32_e32 v154, 1.0, v181
	v_add_f32_e32 v155, 1.0, v176
	v_add_f32_e32 v156, 1.0, v177
	v_mfma_f32_32x32x16_bf16 v[2:17], v[42:45], v[158:161], v[2:17]
	ds_read_b128 v[150:153], v216 offset:16416
	v_fmac_f32_e32 v142, v142, v143
	v_fmac_f32_e32 v154, v154, v144
	v_fmac_f32_e32 v155, v155, v145
	v_fmac_f32_e32 v156, v156, v180
	v_mfma_f32_32x32x16_bf16 v[2:17], v[38:41], v[186:189], v[2:17]
	ds_read_b128 v[174:177], v216 offset:16448
	v_rcp_f32_e32 v142, v142
	v_rcp_f32_e32 v154, v154
	v_rcp_f32_e32 v155, v155
	v_rcp_f32_e32 v156, v156
	v_mfma_f32_32x32x16_bf16 v[2:17], v[34:37], v[190:193], v[2:17]
	ds_read_b128 v[198:201], v216 offset:16480
	v_fma_f32 v142, -v143, v142, v142
	v_fma_f32 v143, -v144, v154, v154
	v_fma_f32 v144, -v145, v155, v155
	v_fma_f32 v145, -v180, v156, v156
	s_waitcnt lgkmcnt(4)
	v_mfma_f32_32x32x16_bf16 v[18:33], v[126:129], v[202:205], v[18:33]
	v_cvt_pk_bf16_f32 v252, v142, v143
	v_cvt_pk_bf16_f32 v253, v144, v145
	v_mfma_f32_32x32x16_bf16 v[18:33], v[122:125], v[194:197], v[18:33]
	s_nop 1
	v_exp_f32_e32 v143, v4
	v_exp_f32_e32 v142, v8
	v_exp_f32_e32 v145, v12
	v_exp_f32_e32 v144, v16
	v_mfma_f32_32x32x16_bf16 v[18:33], v[118:121], v[138:141], v[18:33]
	v_exp_f32_e32 v2, v2
	v_exp_f32_e32 v6, v6
	v_exp_f32_e32 v10, v10
	v_exp_f32_e32 v12, v14
	v_fma_f32 v4, v143, s12, s12
	v_fma_f32 v8, v142, s12, s12
	v_fma_f32 v14, v145, s12, s12
	v_fma_f32 v16, v144, s12, s12
	v_mfma_f32_32x32x16_bf16 v[18:33], v[114:117], v[134:137], v[18:33]
	v_exp_f32_e32 v3, v3
	v_fmac_f32_e32 v4, v2, v4
	v_exp_f32_e32 v2, v7
	v_fmac_f32_e32 v8, v6, v8
	v_exp_f32_e32 v6, v11
	v_exp_f32_e32 v7, v15
	v_fmac_f32_e32 v14, v10, v14
	v_fmac_f32_e32 v16, v12, v16
	v_mfma_f32_32x32x16_bf16 v[18:33], v[110:113], v[166:169], v[18:33]
	v_add_f32_e32 v10, 1.0, v3
	v_rcp_f32_e32 v3, v4
	v_add_f32_e32 v4, 1.0, v2
	v_rcp_f32_e32 v2, v8
	v_rcp_f32_e32 v155, v14
	v_rcp_f32_e32 v154, v16
	v_mfma_f32_32x32x16_bf16 v[18:33], v[106:109], v[162:165], v[18:33]
	v_add_f32_e32 v6, 1.0, v6
	v_add_f32_e32 v7, 1.0, v7
	v_rcp_f32_e32 v157, v10
	v_rcp_f32_e32 v156, v4
	v_exp_f32_e32 v160, v5
	v_exp_f32_e32 v161, v9
	v_mfma_f32_32x32x16_bf16 v[18:33], v[102:105], v[170:173], v[18:33]
	v_rcp_f32_e32 v159, v6
	v_rcp_f32_e32 v158, v7
	v_exp_f32_e32 v180, v13
	v_exp_f32_e32 v181, v17
	v_mfma_f32_32x32x16_bf16 v[18:33], v[98:101], v[130:133], v[18:33]
	v_fma_f32 v142, -v142, v2, v2
	v_fma_f32 v143, -v143, v3, v3
	v_pk_fma_f32 v[216:217], v[156:157], v[206:207], v[142:143]
	v_pk_fma_f32 v[142:143], v[144:145], v[154:155], v[154:155] neg_lo:[1,0,0] neg_hi:[1,0,0]
	s_waitcnt lgkmcnt(0)
	v_mfma_f32_32x32x16_bf16 v[18:33], v[94:97], v[146:149], v[18:33]
	v_pk_fma_f32 v[218:219], v[158:159], v[208:209], v[142:143]
	v_add_f32_e32 v142, 1.0, v160
	v_exp_f32_e32 v143, v217
	v_add_f32_e32 v144, 1.0, v161
	v_exp_f32_e32 v145, v216
	v_exp_f32_e32 v154, v219
	v_exp_f32_e32 v155, v218
	v_add_f32_e32 v156, 1.0, v180
	v_add_f32_e32 v157, 1.0, v181
	v_mfma_f32_32x32x16_bf16 v[18:33], v[90:93], v[150:153], v[18:33]
	v_fmac_f32_e32 v142, v142, v143
	v_fmac_f32_e32 v144, v144, v145
	v_fmac_f32_e32 v156, v156, v154
	v_fmac_f32_e32 v157, v157, v155
	v_mfma_f32_32x32x16_bf16 v[18:33], v[86:89], v[174:177], v[18:33]
	v_rcp_f32_e32 v142, v142
	v_rcp_f32_e32 v144, v144
	v_rcp_f32_e32 v156, v156
	v_rcp_f32_e32 v157, v157
	v_mfma_f32_32x32x16_bf16 v[18:33], v[82:85], v[198:201], v[18:33]
	v_fma_f32 v142, -v143, v142, v142
	v_fma_f32 v143, -v145, v144, v144
	v_fma_f32 v144, -v154, v156, v156
	v_fma_f32 v145, -v155, v157, v157
	v_cvt_pk_bf16_f32 v254, v142, v143
	v_cvt_pk_bf16_f32 v255, v144, v145
	ds_write_b128 v211, v[252:255] offset:8192
	s_waitcnt lgkmcnt(0)
	s_barrier
	v_mfma_f32_32x32x16_bf16 v[2:17], v[78:81], v[202:205], v[236:251]
	v_add_u32_e32 v234, v230, v229
	ds_read2_b32 v[228:229], v232 offset0:64 offset1:96
	ds_read_b128 v[206:209], v210 offset:8192
	v_mfma_f32_32x32x16_bf16 v[2:17], v[74:77], v[194:197], v[2:17]
	ds_read_b128 v[190:193], v210 offset:9216
	v_exp_f32_e32 v179, v20
	v_exp_f32_e32 v178, v24
	v_exp_f32_e32 v181, v28
	v_exp_f32_e32 v180, v32
	v_mfma_f32_32x32x16_bf16 v[2:17], v[70:73], v[138:141], v[2:17]
	ds_read_b128 v[158:161], v210 offset:10240
	v_exp_f32_e32 v18, v18
	v_exp_f32_e32 v22, v22
	v_exp_f32_e32 v24, v26
	v_exp_f32_e32 v26, v30
	v_fma_f32 v20, v179, s12, s12
	v_fma_f32 v28, v178, s12, s12
	v_fma_f32 v30, v181, s12, s12
	v_fma_f32 v32, v180, s12, s12
	v_mfma_f32_32x32x16_bf16 v[2:17], v[66:69], v[134:137], v[2:17]
	ds_read_b128 v[142:145], v210 offset:11264
	v_exp_f32_e32 v19, v19
	v_exp_f32_e32 v23, v23
	v_exp_f32_e32 v27, v27
	v_exp_f32_e32 v31, v31
	v_fmac_f32_e32 v20, v18, v20
	v_fmac_f32_e32 v28, v22, v28
	v_fmac_f32_e32 v30, v24, v30
	v_fmac_f32_e32 v32, v26, v32
	v_mfma_f32_32x32x16_bf16 v[2:17], v[62:65], v[166:169], v[2:17]
	ds_read_b128 v[154:157], v210 offset:12288
	v_add_f32_e32 v22, 1.0, v19
	v_rcp_f32_e32 v19, v20
	v_rcp_f32_e32 v18, v28
	v_rcp_f32_e32 v139, v30
	v_rcp_f32_e32 v138, v32
	v_add_f32_e32 v20, 1.0, v23
	v_mfma_f32_32x32x16_bf16 v[2:17], v[58:61], v[162:165], v[2:17]
	ds_read_b128 v[182:185], v210 offset:13312
	v_rcp_f32_e32 v141, v22
	v_rcp_f32_e32 v140, v20
	v_add_f32_e32 v23, 1.0, v27
	v_add_f32_e32 v20, 1.0, v31
	v_exp_f32_e32 v168, v21
	v_exp_f32_e32 v169, v25
	v_mfma_f32_32x32x16_bf16 v[2:17], v[54:57], v[170:173], v[2:17]
	ds_read_b128 v[186:189], v210 offset:14336
	v_rcp_f32_e32 v163, v23
	v_rcp_f32_e32 v162, v20
	v_exp_f32_e32 v194, v29
	v_exp_f32_e32 v195, v33
	v_mfma_f32_32x32x16_bf16 v[2:17], v[50:53], v[130:133], v[2:17]
	ds_read_b128 v[134:137], v210 offset:15360
	v_fma_f32 v166, -v178, v18, v18
	v_fma_f32 v167, -v179, v19, v19
	ds_read_b128 v[18:21], v231 offset:36928
	ds_read_b128 v[22:25], v231 offset:36944
	ds_read_b128 v[26:29], v231 offset:36960
	ds_read_b128 v[30:33], v231 offset:36976
	v_pk_fma_f32 v[130:131], v[180:181], v[138:139], v[138:139] neg_lo:[1,0,0] neg_hi:[1,0,0]
	v_pk_fma_f32 v[214:215], v[140:141], v[214:215], v[166:167]
	v_pk_fma_f32 v[212:213], v[162:163], v[212:213], v[130:131]
	v_mfma_f32_32x32x16_bf16 v[2:17], v[46:49], v[146:149], v[2:17]
	ds_read_b128 v[138:141], v234 offset:16384
	v_add_f32_e32 v130, 1.0, v168
	v_exp_f32_e32 v131, v215
	v_exp_f32_e32 v132, v214
	v_exp_f32_e32 v133, v213
	v_exp_f32_e32 v162, v212
	v_add_f32_e32 v163, 1.0, v169
	v_add_f32_e32 v166, 1.0, v194
	v_add_f32_e32 v167, 1.0, v195
	v_mfma_f32_32x32x16_bf16 v[2:17], v[42:45], v[150:153], v[2:17]
	ds_read_b128 v[146:149], v234 offset:16416
	v_fmac_f32_e32 v130, v130, v131
	v_fmac_f32_e32 v163, v163, v132
	v_fmac_f32_e32 v166, v166, v133
	v_fmac_f32_e32 v167, v167, v162
	v_mfma_f32_32x32x16_bf16 v[2:17], v[38:41], v[174:177], v[2:17]
	ds_read_b128 v[150:153], v234 offset:16448
	v_rcp_f32_e32 v130, v130
	v_rcp_f32_e32 v163, v163
	v_rcp_f32_e32 v166, v166
	v_rcp_f32_e32 v167, v167
	v_mfma_f32_32x32x16_bf16 v[2:17], v[34:37], v[198:201], v[2:17]
	ds_read_b128 v[178:181], v234 offset:16480
	v_fma_f32 v130, -v131, v130, v130
	v_fma_f32 v131, -v132, v163, v163
	v_fma_f32 v132, -v133, v166, v166
	v_fma_f32 v133, -v162, v167, v167
	s_waitcnt lgkmcnt(4)
	v_mfma_f32_32x32x16_bf16 v[18:33], v[126:129], v[206:209], v[18:33]
	v_cvt_pk_bf16_f32 v252, v130, v131
	v_cvt_pk_bf16_f32 v253, v132, v133
	v_mfma_f32_32x32x16_bf16 v[18:33], v[122:125], v[190:193], v[18:33]
	s_nop 1
	v_exp_f32_e32 v131, v4
	v_exp_f32_e32 v130, v8
	v_exp_f32_e32 v133, v12
	v_exp_f32_e32 v132, v16
	v_mfma_f32_32x32x16_bf16 v[18:33], v[118:121], v[158:161], v[18:33]
	v_exp_f32_e32 v2, v2
	v_exp_f32_e32 v6, v6
	v_exp_f32_e32 v10, v10
	v_exp_f32_e32 v12, v14
	v_fma_f32 v4, v131, s12, s12
	v_fma_f32 v8, v130, s12, s12
	v_fma_f32 v14, v133, s12, s12
	v_fma_f32 v16, v132, s12, s12
	v_mfma_f32_32x32x16_bf16 v[18:33], v[114:117], v[142:145], v[18:33]
	v_exp_f32_e32 v3, v3
	v_fmac_f32_e32 v4, v2, v4
	v_exp_f32_e32 v2, v7
	v_fmac_f32_e32 v8, v6, v8
	v_exp_f32_e32 v6, v11
	v_exp_f32_e32 v7, v15
	v_fmac_f32_e32 v14, v10, v14
	v_fmac_f32_e32 v16, v12, v16
	v_mfma_f32_32x32x16_bf16 v[18:33], v[110:113], v[154:157], v[18:33]
	v_add_f32_e32 v10, 1.0, v3
	v_rcp_f32_e32 v3, v4
	v_add_f32_e32 v4, 1.0, v2
	v_rcp_f32_e32 v2, v8
	v_rcp_f32_e32 v163, v14
	v_rcp_f32_e32 v162, v16
	v_mfma_f32_32x32x16_bf16 v[18:33], v[106:109], v[182:185], v[18:33]
	v_add_f32_e32 v6, 1.0, v6
	v_add_f32_e32 v7, 1.0, v7
	v_rcp_f32_e32 v167, v10
	v_rcp_f32_e32 v166, v4
	v_exp_f32_e32 v170, v5
	v_exp_f32_e32 v171, v9
	v_mfma_f32_32x32x16_bf16 v[18:33], v[102:105], v[186:189], v[18:33]
	v_rcp_f32_e32 v169, v6
	v_rcp_f32_e32 v168, v7
	v_exp_f32_e32 v172, v13
	v_exp_f32_e32 v173, v17
	v_mfma_f32_32x32x16_bf16 v[18:33], v[98:101], v[134:137], v[18:33]
	v_fma_f32 v130, -v130, v2, v2
	v_fma_f32 v131, -v131, v3, v3
	v_pk_fma_f32 v[204:205], v[166:167], v[224:225], v[130:131]
	v_pk_fma_f32 v[130:131], v[132:133], v[162:163], v[162:163] neg_lo:[1,0,0] neg_hi:[1,0,0]
	s_waitcnt lgkmcnt(0)
	v_mfma_f32_32x32x16_bf16 v[18:33], v[94:97], v[138:141], v[18:33]
	v_pk_fma_f32 v[202:203], v[168:169], v[226:227], v[130:131]
	v_add_f32_e32 v130, 1.0, v170
	v_exp_f32_e32 v131, v205
	v_add_f32_e32 v132, 1.0, v171
	v_exp_f32_e32 v133, v204
	v_exp_f32_e32 v162, v203
	v_exp_f32_e32 v163, v202
	v_add_f32_e32 v164, 1.0, v172
	v_add_f32_e32 v165, 1.0, v173
	v_mfma_f32_32x32x16_bf16 v[18:33], v[90:93], v[146:149], v[18:33]
	v_fmac_f32_e32 v130, v130, v131
	v_fmac_f32_e32 v132, v132, v133
	v_fmac_f32_e32 v164, v164, v162
	v_fmac_f32_e32 v165, v165, v163
	v_mfma_f32_32x32x16_bf16 v[18:33], v[86:89], v[150:153], v[18:33]
	v_rcp_f32_e32 v130, v130
	v_rcp_f32_e32 v132, v132
	v_rcp_f32_e32 v164, v164
	v_rcp_f32_e32 v165, v165
	v_mfma_f32_32x32x16_bf16 v[18:33], v[82:85], v[178:181], v[18:33]
	v_fma_f32 v130, -v131, v130, v130
	v_fma_f32 v131, -v133, v132, v132
	v_fma_f32 v132, -v162, v164, v164
	v_fma_f32 v133, -v163, v165, v165
	v_cvt_pk_bf16_f32 v254, v130, v131
	v_cvt_pk_bf16_f32 v255, v132, v133
	ds_write_b128 v211, v[252:255] offset:0
	s_waitcnt lgkmcnt(0)
	s_barrier
	s_branch .LBB1_13
